# MoE P7/P8 main K loops: A-fragment LDS reads issued half a group ahead of their MFMAs, first group's reads issued with the B-fragment reads
# speedup vs baseline: 1.0085x; 1.0069x over previous
; #define MG_STAGE_A(b, rows, k0) do { _Pragma("unroll") for (int h_ = 0; h_ < 2; ++h_) _Pragma("unroll") for (int i_ = 0; i_ < 2; ++i_) if (rows[h_][i_] != 0xffffffffu) \
;         __builtin_amdgcn_global_load_lds((const unsigned*)((const char*)Abase + rows[h_][i_] + (k0) * 2), (PG8_LAS unsigned*)(lds + MG_SA(b, h_) + ldsw + i_ * 8192), 16, 0, 0); } while (0)
; #define MG_LDA(dst, b, h, mp) do { _Pragma("unroll") for (int m = 0; m < 2; ++m) _Pragma("unroll") for (int k = 0; k < 2; ++k) dst[m][k] = *(const PG8_LAS bf16x8*)(lds + MG_SA(b, h) + aoff + (2 * (mp) + m) * 2048 + k * 1024); } while (0)
; #define MG_LDB(dst, b, h) do { _Pragma("unroll") for (int n = 0; n < 2; ++n) _Pragma("unroll") for (int k = 0; k < 2; ++k) dst[n][k] = *(const PG8_LAS bf16x8*)(lds + MG_SB(b, h) + boff + n * 2048 + k * 1024); } while (0)
; #define MG_MMA(ai, bj, mp, At, Bt) do { _Pragma("unroll") for (int m = 0; m < 2; ++m) _Pragma("unroll") for (int n = 0; n < 2; ++n) _Pragma("unroll") for (int k = 0; k < 2; ++k) \
;         acc[ai][bj][2 * (mp) + m][n] = __builtin_amdgcn_mfma_f32_16x16x32_bf16(Bt[n][k], At[m][k], acc[ai][bj][2 * (mp) + m][n], 0, 0, 0); } while (0)
; template <class Epi, bool G1> ...
;     ...
;             if (wact) { MG_LDB(B0, buf, 0); MG_LDB(B1, buf, 1); }
;             if (!last) { MG_STAGE_A(buf ^ 1, rowC, (t + 1) * BK); }
;             else if (has_next) { MG_ROWS(nxt, rowC); MG_STAGE_A(buf ^ 1, rowC, 0); }
;             if (wact) {
; #pragma unroll
;               for (int ai = 0; ai < 2; ++ai)
; #pragma unroll
;                 for (int mp = 0; mp < 2; ++mp) { MG_LDA(At, buf, ai, mp); MG_MMA(ai, 0, mp, At, B0); MG_MMA(ai, 1, mp, At, B1); } }
.LBB0_1082:
	s_add_i32 s46, s71, 0
	s_waitcnt lgkmcnt(0)
	v_add_u32_e32 v168, s46, v218
	v_add_u32_e32 v136, 0x10000, v168
	v_add_u32_e32 v188, 0x14000, v168
	ds_read_b128 v[112:115], v136
	ds_read_b128 v[120:123], v136 offset:1024
	ds_read_b128 v[128:131], v136 offset:2048
	ds_read_b128 v[136:139], v136 offset:3072
	ds_read_b128 v[168:171], v188
	ds_read_b128 v[176:179], v188 offset:1024
	ds_read_b128 v[184:187], v188 offset:2048
	ds_read_b128 v[188:191], v188 offset:3072
	v_add_u32_e32 v244, s71, v219
	ds_read_b128 v[226:229], v244
	ds_read_b128 v[234:237], v244 offset:2048
	ds_read_b128 v[230:233], v244 offset:1024
	ds_read_b128 v[238:241], v244 offset:3072
	s_xor_b32 s72, s71, 0x8000
	s_and_saveexec_b64 s[46:47], s[14:15]
	s_cbranch_execz .LBB0_1077
.LBB0_1083:
	v_lshl_add_u64 v[242:243], s[44:45], 0, v[212:213]
	s_add_i32 m0, s51, s72
	s_nop 0
	global_load_lds_dwordx4 v[242:243], off
	s_or_b64 exec, exec, s[46:47]
	s_and_saveexec_b64 s[46:47], s[12:13]
	s_cbranch_execz .LBB0_1078
.LBB0_1084:
	s_add_i32 s73, s51, s72
	v_lshl_add_u64 v[242:243], s[44:45], 0, v[210:211]
	s_add_i32 m0, s73, 0x2000
	s_nop 0
	global_load_lds_dwordx4 v[242:243], off
	s_or_b64 exec, exec, s[46:47]
	s_and_saveexec_b64 s[46:47], s[8:9]
	s_cbranch_execz .LBB0_1079
.LBB0_1085:
	s_add_i32 s73, s51, s72
	v_lshl_add_u64 v[242:243], s[44:45], 0, v[208:209]
	s_add_i32 m0, s73, 0x4000
	s_nop 0
	global_load_lds_dwordx4 v[242:243], off
	s_or_b64 exec, exec, s[46:47]
	s_and_saveexec_b64 s[46:47], s[6:7]
	s_cbranch_execz .LBB0_1080
.LBB0_1086:
	s_add_i32 s73, s51, s72
	v_lshl_add_u64 v[242:243], s[44:45], 0, v[206:207]
	s_add_i32 m0, s73, 0x6000
	s_nop 0
	global_load_lds_dwordx4 v[242:243], off
	s_or_b64 exec, exec, s[46:47]
	s_and_b64 vcc, exec, s[10:11]
	s_cbranch_vccnz .LBB0_1081
; #define MG_LDA(dst, b, h, mp) do { _Pragma("unroll") for (int m = 0; m < 2; ++m) _Pragma("unroll") for (int k = 0; k < 2; ++k) dst[m][k] = *(const PG8_LAS bf16x8*)(lds + MG_SA(b, h) + aoff + (2 * (mp) + m) * 2048 + k * 1024); } while (0)
; #define MG_MMA(ai, bj, mp, At, Bt) do { _Pragma("unroll") for (int m = 0; m < 2; ++m) _Pragma("unroll") for (int n = 0; n < 2; ++n) _Pragma("unroll") for (int k = 0; k < 2; ++k) \
;         acc[ai][bj][2 * (mp) + m][n] = __builtin_amdgcn_mfma_f32_16x16x32_bf16(Bt[n][k], At[m][k], acc[ai][bj][2 * (mp) + m][n], 0, 0, 0); } while (0)
; template <class Epi, bool G1> ...
;     ...
;             if (wact) {
; #pragma unroll
;               for (int ai = 0; ai < 2; ++ai)
; #pragma unroll
;                 for (int mp = 0; mp < 2; ++mp) { MG_LDA(At, buf, ai, mp); MG_MMA(ai, 0, mp, At, B0); MG_MMA(ai, 1, mp, At, B1); } }
.LBB0_1087:
	s_waitcnt lgkmcnt(2)
	v_mfma_f32_16x16x32_bf16 v[180:183], v[112:115], v[226:229], v[180:183]
	v_mfma_f32_16x16x32_bf16 v[172:175], v[128:131], v[226:229], v[172:175]
	v_mfma_f32_16x16x32_bf16 v[164:167], v[112:115], v[234:237], v[164:167]
	v_mfma_f32_16x16x32_bf16 v[160:163], v[128:131], v[234:237], v[160:163]
	v_mfma_f32_16x16x32_bf16 v[140:143], v[168:171], v[226:229], v[140:143]
	v_mfma_f32_16x16x32_bf16 v[132:135], v[184:187], v[226:229], v[132:135]
	v_mfma_f32_16x16x32_bf16 v[124:127], v[168:171], v[234:237], v[124:127]
	v_mfma_f32_16x16x32_bf16 v[116:119], v[184:187], v[234:237], v[116:119]
	ds_read_b128 v[226:229], v244 offset:4096
	ds_read_b128 v[234:237], v244 offset:6144
	s_waitcnt lgkmcnt(2)
	v_mfma_f32_16x16x32_bf16 v[180:183], v[120:123], v[230:233], v[180:183]
	v_mfma_f32_16x16x32_bf16 v[172:175], v[136:139], v[230:233], v[172:175]
	v_mfma_f32_16x16x32_bf16 v[164:167], v[120:123], v[238:241], v[164:167]
	v_mfma_f32_16x16x32_bf16 v[160:163], v[136:139], v[238:241], v[160:163]
	v_mfma_f32_16x16x32_bf16 v[140:143], v[176:179], v[230:233], v[140:143]
	v_mfma_f32_16x16x32_bf16 v[132:135], v[188:191], v[230:233], v[132:135]
	v_mfma_f32_16x16x32_bf16 v[124:127], v[176:179], v[238:241], v[124:127]
	v_mfma_f32_16x16x32_bf16 v[116:119], v[188:191], v[238:241], v[116:119]
	ds_read_b128 v[230:233], v244 offset:5120
	ds_read_b128 v[238:241], v244 offset:7168
	s_waitcnt lgkmcnt(2)
	v_mfma_f32_16x16x32_bf16 v[156:159], v[112:115], v[226:229], v[156:159]
	v_mfma_f32_16x16x32_bf16 v[152:155], v[128:131], v[226:229], v[152:155]
	v_mfma_f32_16x16x32_bf16 v[148:151], v[112:115], v[234:237], v[148:151]
	v_mfma_f32_16x16x32_bf16 v[144:147], v[128:131], v[234:237], v[144:147]
	v_mfma_f32_16x16x32_bf16 v[108:111], v[168:171], v[226:229], v[108:111]
	v_mfma_f32_16x16x32_bf16 v[104:107], v[184:187], v[226:229], v[104:107]
	v_mfma_f32_16x16x32_bf16 v[100:103], v[168:171], v[234:237], v[100:103]
	v_mfma_f32_16x16x32_bf16 v[96:99], v[184:187], v[234:237], v[96:99]
	ds_read_b128 v[226:229], v244 offset:16384
	ds_read_b128 v[234:237], v244 offset:18432
	s_waitcnt lgkmcnt(2)
	v_mfma_f32_16x16x32_bf16 v[156:159], v[120:123], v[230:233], v[156:159]
	v_mfma_f32_16x16x32_bf16 v[152:155], v[136:139], v[230:233], v[152:155]
	v_mfma_f32_16x16x32_bf16 v[148:151], v[120:123], v[238:241], v[148:151]
	v_mfma_f32_16x16x32_bf16 v[144:147], v[136:139], v[238:241], v[144:147]
	v_mfma_f32_16x16x32_bf16 v[108:111], v[176:179], v[230:233], v[108:111]
	v_mfma_f32_16x16x32_bf16 v[104:107], v[188:191], v[230:233], v[104:107]
	v_mfma_f32_16x16x32_bf16 v[100:103], v[176:179], v[238:241], v[100:103]
	v_mfma_f32_16x16x32_bf16 v[96:99], v[188:191], v[238:241], v[96:99]
	ds_read_b128 v[230:233], v244 offset:17408
	ds_read_b128 v[238:241], v244 offset:19456
	s_waitcnt lgkmcnt(2)
	v_mfma_f32_16x16x32_bf16 v[92:95], v[112:115], v[226:229], v[92:95]
	v_mfma_f32_16x16x32_bf16 v[88:91], v[128:131], v[226:229], v[88:91]
	v_mfma_f32_16x16x32_bf16 v[84:87], v[112:115], v[234:237], v[84:87]
	v_mfma_f32_16x16x32_bf16 v[80:83], v[128:131], v[234:237], v[80:83]
	v_mfma_f32_16x16x32_bf16 v[60:63], v[168:171], v[226:229], v[60:63]
	v_mfma_f32_16x16x32_bf16 v[56:59], v[184:187], v[226:229], v[56:59]
	v_mfma_f32_16x16x32_bf16 v[52:55], v[168:171], v[234:237], v[52:55]
	v_mfma_f32_16x16x32_bf16 v[48:51], v[184:187], v[234:237], v[48:51]
	ds_read_b128 v[226:229], v244 offset:20480
	ds_read_b128 v[234:237], v244 offset:22528
	s_waitcnt lgkmcnt(2)
	v_mfma_f32_16x16x32_bf16 v[92:95], v[120:123], v[230:233], v[92:95]
	v_mfma_f32_16x16x32_bf16 v[88:91], v[136:139], v[230:233], v[88:91]
	v_mfma_f32_16x16x32_bf16 v[84:87], v[120:123], v[238:241], v[84:87]
	v_mfma_f32_16x16x32_bf16 v[80:83], v[136:139], v[238:241], v[80:83]
	v_mfma_f32_16x16x32_bf16 v[60:63], v[176:179], v[230:233], v[60:63]
	v_mfma_f32_16x16x32_bf16 v[56:59], v[188:191], v[230:233], v[56:59]
	v_mfma_f32_16x16x32_bf16 v[52:55], v[176:179], v[238:241], v[52:55]
	v_mfma_f32_16x16x32_bf16 v[48:51], v[188:191], v[238:241], v[48:51]
	ds_read_b128 v[230:233], v244 offset:21504
	ds_read_b128 v[238:241], v244 offset:23552
	s_waitcnt lgkmcnt(2)
	v_mfma_f32_16x16x32_bf16 v[76:79], v[112:115], v[226:229], v[76:79]
	v_mfma_f32_16x16x32_bf16 v[72:75], v[128:131], v[226:229], v[72:75]
	v_mfma_f32_16x16x32_bf16 v[68:71], v[112:115], v[234:237], v[68:71]
	v_mfma_f32_16x16x32_bf16 v[64:67], v[128:131], v[234:237], v[64:67]
	v_mfma_f32_16x16x32_bf16 v[40:43], v[168:171], v[226:229], v[40:43]
	v_mfma_f32_16x16x32_bf16 v[36:39], v[184:187], v[226:229], v[36:39]
	v_mfma_f32_16x16x32_bf16 v[32:35], v[168:171], v[234:237], v[32:35]
	v_mfma_f32_16x16x32_bf16 v[24:27], v[184:187], v[234:237], v[24:27]
	s_waitcnt lgkmcnt(0)
	v_mfma_f32_16x16x32_bf16 v[76:79], v[120:123], v[230:233], v[76:79]
	v_mfma_f32_16x16x32_bf16 v[72:75], v[136:139], v[230:233], v[72:75]
	v_mfma_f32_16x16x32_bf16 v[68:71], v[120:123], v[238:241], v[68:71]
	v_mfma_f32_16x16x32_bf16 v[64:67], v[136:139], v[238:241], v[64:67]
	v_mfma_f32_16x16x32_bf16 v[40:43], v[176:179], v[230:233], v[40:43]
	v_mfma_f32_16x16x32_bf16 v[36:39], v[188:191], v[230:233], v[36:39]
	v_mfma_f32_16x16x32_bf16 v[32:35], v[176:179], v[238:241], v[32:35]
	v_mfma_f32_16x16x32_bf16 v[24:27], v[188:191], v[238:241], v[24:27]
	s_and_saveexec_b64 s[46:47], s[20:21]
	s_cbranch_execz .LBB0_1074

; #define MG_STAGE_A(b, rows, k0) do { _Pragma("unroll") for (int h_ = 0; h_ < 2; ++h_) _Pragma("unroll") for (int i_ = 0; i_ < 2; ++i_) if (rows[h_][i_] != 0xffffffffu) \
;         __builtin_amdgcn_global_load_lds((const unsigned*)((const char*)Abase + rows[h_][i_] + (k0) * 2), (PG8_LAS unsigned*)(lds + MG_SA(b, h_) + ldsw + i_ * 8192), 16, 0, 0); } while (0)
; #define MG_LDA(dst, b, h, mp) do { _Pragma("unroll") for (int m = 0; m < 2; ++m) _Pragma("unroll") for (int k = 0; k < 2; ++k) dst[m][k] = *(const PG8_LAS bf16x8*)(lds + MG_SA(b, h) + aoff + (2 * (mp) + m) * 2048 + k * 1024); } while (0)
; #define MG_LDB(dst, b, h) do { _Pragma("unroll") for (int n = 0; n < 2; ++n) _Pragma("unroll") for (int k = 0; k < 2; ++k) dst[n][k] = *(const PG8_LAS bf16x8*)(lds + MG_SB(b, h) + boff + n * 2048 + k * 1024); } while (0)
; #define MG_MMA(ai, bj, mp, At, Bt) do { _Pragma("unroll") for (int m = 0; m < 2; ++m) _Pragma("unroll") for (int n = 0; n < 2; ++n) _Pragma("unroll") for (int k = 0; k < 2; ++k) \
;         acc[ai][bj][2 * (mp) + m][n] = __builtin_amdgcn_mfma_f32_16x16x32_bf16(Bt[n][k], At[m][k], acc[ai][bj][2 * (mp) + m][n], 0, 0, 0); } while (0)
; template <class Epi, bool G1> ...
;     ...
;             if (wact) { MG_LDB(B0, buf, 0); MG_LDB(B1, buf, 1); }
;             if (!last) { MG_STAGE_A(buf ^ 1, rowC, (t + 1) * BK); }
;             else if (has_next) { MG_ROWS(nxt, rowC); MG_STAGE_A(buf ^ 1, rowC, 0); }
;             if (wact) {
; #pragma unroll
;               for (int ai = 0; ai < 2; ++ai)
; #pragma unroll
;                 for (int mp = 0; mp < 2; ++mp) { MG_LDA(At, buf, ai, mp); MG_MMA(ai, 0, mp, At, B0); MG_MMA(ai, 1, mp, At, B1); } }
.LBB0_1271:
	s_add_i32 s52, s74, 0
	s_waitcnt lgkmcnt(0)
	v_add_u32_e32 v172, s52, v220
	v_add_u32_e32 v140, 0x10000, v172
	v_add_u32_e32 v192, 0x14000, v172
	ds_read_b128 v[116:119], v140
	ds_read_b128 v[124:127], v140 offset:1024
	ds_read_b128 v[132:135], v140 offset:2048
	ds_read_b128 v[140:143], v140 offset:3072
	ds_read_b128 v[172:175], v192
	ds_read_b128 v[180:183], v192 offset:1024
	ds_read_b128 v[188:191], v192 offset:2048
	ds_read_b128 v[192:195], v192 offset:3072
	v_add_u32_e32 v244, s74, v221
	ds_read_b128 v[226:229], v244
	ds_read_b128 v[234:237], v244 offset:2048
	ds_read_b128 v[230:233], v244 offset:1024
	ds_read_b128 v[238:241], v244 offset:3072
	s_xor_b32 s75, s74, 0x8000
	s_and_saveexec_b64 s[52:53], s[14:15]
	s_cbranch_execz .LBB0_1266
.LBB0_1272:
	v_lshl_add_u64 v[242:243], s[50:51], 0, v[212:213]
	s_add_i32 m0, s57, s75
	s_nop 0
	global_load_lds_dwordx4 v[242:243], off
	s_or_b64 exec, exec, s[52:53]
	s_and_saveexec_b64 s[52:53], s[12:13]
	s_cbranch_execz .LBB0_1267
.LBB0_1273:
	s_add_i32 s76, s57, s75
	v_lshl_add_u64 v[242:243], s[50:51], 0, v[210:211]
	s_add_i32 m0, s76, 0x2000
	s_nop 0
	global_load_lds_dwordx4 v[242:243], off
	s_or_b64 exec, exec, s[52:53]
	s_and_saveexec_b64 s[52:53], s[8:9]
	s_cbranch_execz .LBB0_1268
.LBB0_1274:
	s_add_i32 s76, s57, s75
	v_lshl_add_u64 v[242:243], s[50:51], 0, v[208:209]
	s_add_i32 m0, s76, 0x4000
	s_nop 0
	global_load_lds_dwordx4 v[242:243], off
	s_or_b64 exec, exec, s[52:53]
	s_and_saveexec_b64 s[52:53], s[6:7]
	s_cbranch_execz .LBB0_1269
.LBB0_1275:
	s_add_i32 s76, s57, s75
	v_lshl_add_u64 v[242:243], s[50:51], 0, v[2:3]
	s_add_i32 m0, s76, 0x6000
	s_nop 0
	global_load_lds_dwordx4 v[242:243], off
	s_or_b64 exec, exec, s[52:53]
	s_and_b64 vcc, exec, s[10:11]
	s_cbranch_vccnz .LBB0_1270
; #define MG_LDA(dst, b, h, mp) do { _Pragma("unroll") for (int m = 0; m < 2; ++m) _Pragma("unroll") for (int k = 0; k < 2; ++k) dst[m][k] = *(const PG8_LAS bf16x8*)(lds + MG_SA(b, h) + aoff + (2 * (mp) + m) * 2048 + k * 1024); } while (0)
; #define MG_MMA(ai, bj, mp, At, Bt) do { _Pragma("unroll") for (int m = 0; m < 2; ++m) _Pragma("unroll") for (int n = 0; n < 2; ++n) _Pragma("unroll") for (int k = 0; k < 2; ++k) \
;         acc[ai][bj][2 * (mp) + m][n] = __builtin_amdgcn_mfma_f32_16x16x32_bf16(Bt[n][k], At[m][k], acc[ai][bj][2 * (mp) + m][n], 0, 0, 0); } while (0)
; template <class Epi, bool G1> ...
;     ...
;             if (wact) {
; #pragma unroll
;               for (int ai = 0; ai < 2; ++ai)
; #pragma unroll
;                 for (int mp = 0; mp < 2; ++mp) { MG_LDA(At, buf, ai, mp); MG_MMA(ai, 0, mp, At, B0); MG_MMA(ai, 1, mp, At, B1); } }
.LBB0_1276:
	s_waitcnt lgkmcnt(2)
	v_mfma_f32_16x16x32_bf16 v[184:187], v[116:119], v[226:229], v[184:187]
	v_mfma_f32_16x16x32_bf16 v[176:179], v[132:135], v[226:229], v[176:179]
	v_mfma_f32_16x16x32_bf16 v[168:171], v[116:119], v[234:237], v[168:171]
	v_mfma_f32_16x16x32_bf16 v[164:167], v[132:135], v[234:237], v[164:167]
	v_mfma_f32_16x16x32_bf16 v[144:147], v[172:175], v[226:229], v[144:147]
	v_mfma_f32_16x16x32_bf16 v[136:139], v[188:191], v[226:229], v[136:139]
	v_mfma_f32_16x16x32_bf16 v[128:131], v[172:175], v[234:237], v[128:131]
	v_mfma_f32_16x16x32_bf16 v[120:123], v[188:191], v[234:237], v[120:123]
	ds_read_b128 v[226:229], v244 offset:4096
	ds_read_b128 v[234:237], v244 offset:6144
	s_waitcnt lgkmcnt(2)
	v_mfma_f32_16x16x32_bf16 v[184:187], v[124:127], v[230:233], v[184:187]
	v_mfma_f32_16x16x32_bf16 v[176:179], v[140:143], v[230:233], v[176:179]
	v_mfma_f32_16x16x32_bf16 v[168:171], v[124:127], v[238:241], v[168:171]
	v_mfma_f32_16x16x32_bf16 v[164:167], v[140:143], v[238:241], v[164:167]
	v_mfma_f32_16x16x32_bf16 v[144:147], v[180:183], v[230:233], v[144:147]
	v_mfma_f32_16x16x32_bf16 v[136:139], v[192:195], v[230:233], v[136:139]
	v_mfma_f32_16x16x32_bf16 v[128:131], v[180:183], v[238:241], v[128:131]
	v_mfma_f32_16x16x32_bf16 v[120:123], v[192:195], v[238:241], v[120:123]
	ds_read_b128 v[230:233], v244 offset:5120
	ds_read_b128 v[238:241], v244 offset:7168
	s_waitcnt lgkmcnt(2)
	v_mfma_f32_16x16x32_bf16 v[160:163], v[116:119], v[226:229], v[160:163]
	v_mfma_f32_16x16x32_bf16 v[156:159], v[132:135], v[226:229], v[156:159]
	v_mfma_f32_16x16x32_bf16 v[152:155], v[116:119], v[234:237], v[152:155]
	v_mfma_f32_16x16x32_bf16 v[148:151], v[132:135], v[234:237], v[148:151]
	v_mfma_f32_16x16x32_bf16 v[112:115], v[172:175], v[226:229], v[112:115]
	v_mfma_f32_16x16x32_bf16 v[108:111], v[188:191], v[226:229], v[108:111]
	v_mfma_f32_16x16x32_bf16 v[104:107], v[172:175], v[234:237], v[104:107]
	v_mfma_f32_16x16x32_bf16 v[100:103], v[188:191], v[234:237], v[100:103]
	ds_read_b128 v[226:229], v244 offset:16384
	ds_read_b128 v[234:237], v244 offset:18432
	s_waitcnt lgkmcnt(2)
	v_mfma_f32_16x16x32_bf16 v[160:163], v[124:127], v[230:233], v[160:163]
	v_mfma_f32_16x16x32_bf16 v[156:159], v[140:143], v[230:233], v[156:159]
	v_mfma_f32_16x16x32_bf16 v[152:155], v[124:127], v[238:241], v[152:155]
	v_mfma_f32_16x16x32_bf16 v[148:151], v[140:143], v[238:241], v[148:151]
	v_mfma_f32_16x16x32_bf16 v[112:115], v[180:183], v[230:233], v[112:115]
	v_mfma_f32_16x16x32_bf16 v[108:111], v[192:195], v[230:233], v[108:111]
	v_mfma_f32_16x16x32_bf16 v[104:107], v[180:183], v[238:241], v[104:107]
	v_mfma_f32_16x16x32_bf16 v[100:103], v[192:195], v[238:241], v[100:103]
	ds_read_b128 v[230:233], v244 offset:17408
	ds_read_b128 v[238:241], v244 offset:19456
	s_waitcnt lgkmcnt(2)
	v_mfma_f32_16x16x32_bf16 v[96:99], v[116:119], v[226:229], v[96:99]
	v_mfma_f32_16x16x32_bf16 v[92:95], v[132:135], v[226:229], v[92:95]
	v_mfma_f32_16x16x32_bf16 v[88:91], v[116:119], v[234:237], v[88:91]
	v_mfma_f32_16x16x32_bf16 v[84:87], v[132:135], v[234:237], v[84:87]
	v_mfma_f32_16x16x32_bf16 v[64:67], v[172:175], v[226:229], v[64:67]
	v_mfma_f32_16x16x32_bf16 v[60:63], v[188:191], v[226:229], v[60:63]
	v_mfma_f32_16x16x32_bf16 v[52:55], v[172:175], v[234:237], v[52:55]
	v_mfma_f32_16x16x32_bf16 v[48:51], v[188:191], v[234:237], v[48:51]
	ds_read_b128 v[226:229], v244 offset:20480
	ds_read_b128 v[234:237], v244 offset:22528
	s_waitcnt lgkmcnt(2)
	v_mfma_f32_16x16x32_bf16 v[96:99], v[124:127], v[230:233], v[96:99]
	v_mfma_f32_16x16x32_bf16 v[92:95], v[140:143], v[230:233], v[92:95]
	v_mfma_f32_16x16x32_bf16 v[88:91], v[124:127], v[238:241], v[88:91]
	v_mfma_f32_16x16x32_bf16 v[84:87], v[140:143], v[238:241], v[84:87]
	v_mfma_f32_16x16x32_bf16 v[64:67], v[180:183], v[230:233], v[64:67]
	v_mfma_f32_16x16x32_bf16 v[60:63], v[192:195], v[230:233], v[60:63]
	v_mfma_f32_16x16x32_bf16 v[52:55], v[180:183], v[238:241], v[52:55]
	v_mfma_f32_16x16x32_bf16 v[48:51], v[192:195], v[238:241], v[48:51]
	ds_read_b128 v[230:233], v244 offset:21504
	ds_read_b128 v[238:241], v244 offset:23552
	s_waitcnt lgkmcnt(2)
	v_mfma_f32_16x16x32_bf16 v[80:83], v[116:119], v[226:229], v[80:83]
	v_mfma_f32_16x16x32_bf16 v[76:79], v[132:135], v[226:229], v[76:79]
	v_mfma_f32_16x16x32_bf16 v[72:75], v[116:119], v[234:237], v[72:75]
	v_mfma_f32_16x16x32_bf16 v[68:71], v[132:135], v[234:237], v[68:71]
	v_mfma_f32_16x16x32_bf16 v[44:47], v[172:175], v[226:229], v[44:47]
	v_mfma_f32_16x16x32_bf16 v[40:43], v[188:191], v[226:229], v[40:43]
	v_mfma_f32_16x16x32_bf16 v[36:39], v[172:175], v[234:237], v[36:39]
	v_mfma_f32_16x16x32_bf16 v[32:35], v[188:191], v[234:237], v[32:35]
	s_waitcnt lgkmcnt(0)
	v_mfma_f32_16x16x32_bf16 v[80:83], v[124:127], v[230:233], v[80:83]
	v_mfma_f32_16x16x32_bf16 v[76:79], v[140:143], v[230:233], v[76:79]
	v_mfma_f32_16x16x32_bf16 v[72:75], v[124:127], v[238:241], v[72:75]
	v_mfma_f32_16x16x32_bf16 v[68:71], v[140:143], v[238:241], v[68:71]
	v_mfma_f32_16x16x32_bf16 v[44:47], v[180:183], v[230:233], v[44:47]
	v_mfma_f32_16x16x32_bf16 v[40:43], v[192:195], v[230:233], v[40:43]
	v_mfma_f32_16x16x32_bf16 v[36:39], v[180:183], v[238:241], v[36:39]
	v_mfma_f32_16x16x32_bf16 v[32:35], v[192:195], v[238:241], v[32:35]
	s_and_saveexec_b64 s[52:53], s[22:23]
	s_cbranch_execz .LBB0_1263
